# baseline (speedup 1.0000x reference)
_Z5k_aggPKDF16_PKhPKiS4_PKDv8_DF16_PKfPDF16_Pf:
	s_load_dwordx8 s[4:11], s[0:1], 0x8
	s_load_dwordx4 s[12:15], s[0:1], 0x28
	s_load_dwordx2 s[16:17], s[0:1], 0x38
	v_lshlrev_b32_e32 v2, 4, v0
	s_lshl_b32 s0, s2, 2
	s_lshl_b32 s1, s2, 3
	s_andn2_b32 s0, s0, 63
	s_and_b32 s1, s1, 56
	s_or_b32 s0, s0, s1
	s_lshr_b32 s1, s2, 1
	s_and_b32 s1, s1, 4
	s_or_b32 s0, s0, s1
	v_lshlrev_b32_e32 v1, 2, v0
	v_lshrrev_b32_e32 v52, 6, v0
	v_or_b32_e32 v3, s0, v52
	v_mov_b32_e32 v98, v2
	s_waitcnt lgkmcnt(0)
	v_readfirstlane_b32 s19, v52
	s_nop 3
	s_lshl_b32 s19, s19, 10
	s_mov_b32 m0, s19
	s_nop 0
	global_load_lds_dwordx4 v2, s[10:11]
	s_add_u32 m0, s19, 0x1000
	v_add_u32_e32 v96, 0x1000, v2
	global_load_lds_dwordx4 v96, s[10:11]
	s_add_u32 m0, s19, 0x2000
	v_add_u32_e32 v96, 0x2000, v2
	global_load_lds_dwordx4 v96, s[10:11]
	s_add_u32 m0, s19, 0x3000
	v_add_u32_e32 v96, 0x3000, v2
	global_load_lds_dwordx4 v96, s[10:11]
	s_add_u32 m0, s19, 0x4000
	v_add_u32_e32 v96, 0x4000, v2
	global_load_lds_dwordx4 v96, s[10:11]
	s_add_u32 m0, s19, 0x5000
	v_add_u32_e32 v96, 0x5000, v2
	global_load_lds_dwordx4 v96, s[10:11]
	s_add_u32 m0, s19, 0x6000
	v_add_u32_e32 v96, 0x6000, v2
	global_load_lds_dwordx4 v96, s[10:11]
	s_add_u32 m0, s19, 0x7000
	v_add_u32_e32 v96, 0x7000, v2
	global_load_lds_dwordx4 v96, s[10:11]
	v_mov_b32_e32 v97, 0
	ds_write2st64_b32 v1, v97, v97 offset0:128 offset1:132
	ds_write2st64_b32 v1, v97, v97 offset0:136 offset1:140
	s_movk_i32 s0, 0x186a
	v_cmp_gt_i32_e32 vcc, s0, v3
	s_and_saveexec_b64 s[0:1], vcc
	s_cbranch_execz .Lagg_invalid
	v_bfe_u32 v4, v0, 2, 4
	v_lshlrev_b32_e32 v53, 4, v3
	v_or_b32_e32 v10, v53, v4
	v_and_b32_e32 v54, 48, v2
	v_lshl_or_b32 v11, v10, 7, v54
	global_load_dwordx4 v[2:5], v11, s[4:5]
	global_load_dwordx4 v[6:9], v11, s[4:5] offset:64
	v_ashrrev_i32_e32 v11, 31, v10
	v_lshl_add_u64 v[10:11], v[10:11], 2, s[6:7]
	global_load_dwordx2 v[50:51], v[10:11], off
	s_waitcnt vmcnt(2)
	v_cvt_pk_f32_fp8_e32 v[10:11], v2
	v_cvt_pk_f32_fp8_sdwa v[12:13], v2 src0_sel:WORD_1
	v_cvt_pk_f32_fp8_e32 v[14:15], v3
	v_cvt_pk_f32_fp8_sdwa v[2:3], v3 src0_sel:WORD_1
	v_cvt_pk_f32_fp8_e32 v[16:17], v4
	v_cvt_pk_f32_fp8_sdwa v[18:19], v4 src0_sel:WORD_1
	v_cvt_pk_f32_fp8_e32 v[20:21], v5
	v_cvt_pk_f32_fp8_sdwa v[4:5], v5 src0_sel:WORD_1
	s_waitcnt vmcnt(1)
	v_cvt_pk_f32_fp8_e32 v[22:23], v6
	v_cvt_pk_f32_fp8_sdwa v[24:25], v6 src0_sel:WORD_1
	v_cvt_pk_f32_fp8_e32 v[26:27], v7
	v_cvt_pk_f32_fp8_sdwa v[6:7], v7 src0_sel:WORD_1
	v_cvt_pk_f32_fp8_e32 v[28:29], v8
	v_cvt_pk_f32_fp8_sdwa v[30:31], v8 src0_sel:WORD_1
	v_cvt_pk_f32_fp8_e32 v[32:33], v9
	v_cvt_pk_f32_fp8_sdwa v[8:9], v9 src0_sel:WORD_1
	v_add_f32_e32 v88, 0, v10
	v_add_f32_e32 v89, 0, v11
	v_add_f32_e32 v90, 0, v12
	v_add_f32_e32 v91, 0, v13
	v_add_f32_e32 v92, 0, v14
	v_add_f32_e32 v93, 0, v15
	v_add_f32_e32 v94, 0, v2
	v_add_f32_e32 v95, 0, v3
	v_add_f32_e32 v76, 0, v16
	v_add_f32_e32 v77, 0, v17
	v_add_f32_e32 v80, 0, v18
	v_add_f32_e32 v81, 0, v19
	v_add_f32_e32 v84, 0, v20
	v_add_f32_e32 v85, 0, v21
	v_add_f32_e32 v86, 0, v4
	v_add_f32_e32 v87, 0, v5
	v_add_f32_e32 v72, 0, v22
	v_add_f32_e32 v73, 0, v23
	v_add_f32_e32 v74, 0, v24
	v_add_f32_e32 v75, 0, v25
	v_add_f32_e32 v78, 0, v26
	v_add_f32_e32 v79, 0, v27
	v_add_f32_e32 v82, 0, v6
	v_add_f32_e32 v83, 0, v7
	v_add_f32_e32 v64, 0, v28
	v_add_f32_e32 v65, 0, v29
	v_add_f32_e32 v66, 0, v30
	v_add_f32_e32 v67, 0, v31
	v_add_f32_e32 v68, 0, v32
	v_add_f32_e32 v69, 0, v33
	v_add_f32_e32 v70, 0, v8
	v_add_f32_e32 v71, 0, v9
	s_waitcnt vmcnt(0)
	s_mov_b64 s[6:7], exec
	v_mov_b32_e32 v63, 0xc35000
	v_add_u32_e32 v106, 0, v50
	v_lshlrev_b32_e32 v106, 2, v106
	global_load_dwordx3 v[56:58], v106, s[8:9]
	v_add_u32_e32 v106, 3, v50
	v_lshlrev_b32_e32 v106, 2, v106
	global_load_dwordx3 v[60:62], v106, s[8:9]
	s_waitcnt vmcnt(0)
	v_add_u32_e32 v104, 0, v50
	v_cmp_lt_i32_e32 vcc, v104, v51
	v_lshlrev_b32_e32 v105, 7, v56
	s_nop 0
	v_cndmask_b32_e32 v105, v63, v105, vcc
	v_or_b32_e32 v105, v54, v105
	global_load_dwordx4 v[2:5], v105, s[4:5]
	global_load_dwordx4 v[6:9], v105, s[4:5] offset:64
	v_add_u32_e32 v104, 1, v50
	v_cmp_lt_i32_e32 vcc, v104, v51
	v_lshlrev_b32_e32 v105, 7, v57
	s_nop 0
	v_cndmask_b32_e32 v105, v63, v105, vcc
	v_or_b32_e32 v105, v54, v105
	global_load_dwordx4 v[10:13], v105, s[4:5]
	global_load_dwordx4 v[14:17], v105, s[4:5] offset:64
	v_add_u32_e32 v104, 2, v50
	v_cmp_lt_i32_e32 vcc, v104, v51
	v_lshlrev_b32_e32 v105, 7, v58
	s_nop 0
	v_cndmask_b32_e32 v105, v63, v105, vcc
	v_or_b32_e32 v105, v54, v105
	global_load_dwordx4 v[18:21], v105, s[4:5]
	global_load_dwordx4 v[22:25], v105, s[4:5] offset:64
	v_add_u32_e32 v106, 6, v50
	v_lshlrev_b32_e32 v106, 2, v106
	global_load_dwordx3 v[56:58], v106, s[8:9]
	v_add_u32_e32 v104, 3, v50
	v_cmp_lt_i32_e32 vcc, v104, v51
	v_lshlrev_b32_e32 v105, 7, v60
	s_nop 0
	v_cndmask_b32_e32 v105, v63, v105, vcc
	v_or_b32_e32 v105, v54, v105
	global_load_dwordx4 v[26:29], v105, s[4:5]
	global_load_dwordx4 v[30:33], v105, s[4:5] offset:64
	v_add_u32_e32 v104, 4, v50
	v_cmp_lt_i32_e32 vcc, v104, v51
	v_lshlrev_b32_e32 v105, 7, v61
	s_nop 0
	v_cndmask_b32_e32 v105, v63, v105, vcc
	v_or_b32_e32 v105, v54, v105
	global_load_dwordx4 v[34:37], v105, s[4:5]
	global_load_dwordx4 v[38:41], v105, s[4:5] offset:64
	v_add_u32_e32 v104, 5, v50
	v_cmp_lt_i32_e32 vcc, v104, v51
	v_lshlrev_b32_e32 v105, 7, v62
	s_nop 0
	v_cndmask_b32_e32 v105, v63, v105, vcc
	v_or_b32_e32 v105, v54, v105
	global_load_dwordx4 v[42:45], v105, s[4:5]
	global_load_dwordx4 v[46:49], v105, s[4:5] offset:64
	v_add_u32_e32 v106, 9, v50
	v_lshlrev_b32_e32 v106, 2, v106
	global_load_dwordx3 v[60:62], v106, s[8:9]
	v_add_u32_e32 v104, 6, v50
	v_cmp_lt_i32_e32 vcc, v104, v51
	s_and_b64 vcc, exec, vcc
	s_cbranch_scc0 .Lagg_glast
.Lagg_gloop:
	s_waitcnt vmcnt(7)
	v_cvt_pk_f32_fp8_e32 v[96:97], v2
	v_cvt_pk_f32_fp8_sdwa v[98:99], v2 src0_sel:WORD_1
	v_cvt_pk_f32_fp8_e32 v[100:101], v3
	v_cvt_pk_f32_fp8_sdwa v[102:103], v3 src0_sel:WORD_1
	v_pk_add_f32 v[88:89], v[88:89], v[96:97]
	v_pk_add_f32 v[90:91], v[90:91], v[98:99]
	v_pk_add_f32 v[92:93], v[92:93], v[100:101]
	v_pk_add_f32 v[94:95], v[94:95], v[102:103]
	v_cvt_pk_f32_fp8_e32 v[96:97], v4
	v_cvt_pk_f32_fp8_sdwa v[98:99], v4 src0_sel:WORD_1
	v_cvt_pk_f32_fp8_e32 v[100:101], v5
	v_cvt_pk_f32_fp8_sdwa v[102:103], v5 src0_sel:WORD_1
	v_pk_add_f32 v[76:77], v[76:77], v[96:97]
	v_pk_add_f32 v[80:81], v[80:81], v[98:99]
	v_pk_add_f32 v[84:85], v[84:85], v[100:101]
	v_pk_add_f32 v[86:87], v[86:87], v[102:103]
	v_cvt_pk_f32_fp8_e32 v[96:97], v6
	v_cvt_pk_f32_fp8_sdwa v[98:99], v6 src0_sel:WORD_1
	v_cvt_pk_f32_fp8_e32 v[100:101], v7
	v_cvt_pk_f32_fp8_sdwa v[102:103], v7 src0_sel:WORD_1
	v_pk_add_f32 v[72:73], v[72:73], v[96:97]
	v_pk_add_f32 v[74:75], v[74:75], v[98:99]
	v_pk_add_f32 v[78:79], v[78:79], v[100:101]
	v_pk_add_f32 v[82:83], v[82:83], v[102:103]
	v_cvt_pk_f32_fp8_e32 v[96:97], v8
	v_cvt_pk_f32_fp8_sdwa v[98:99], v8 src0_sel:WORD_1
	v_cvt_pk_f32_fp8_e32 v[100:101], v9
	v_cvt_pk_f32_fp8_sdwa v[102:103], v9 src0_sel:WORD_1
	v_pk_add_f32 v[64:65], v[64:65], v[96:97]
	v_pk_add_f32 v[66:67], v[66:67], v[98:99]
	v_pk_add_f32 v[68:69], v[68:69], v[100:101]
	v_pk_add_f32 v[70:71], v[70:71], v[102:103]
	v_add_u32_e32 v104, 6, v50
	v_cmp_lt_i32_e32 vcc, v104, v51
	v_lshlrev_b32_e32 v105, 7, v56
	s_nop 0
	v_cndmask_b32_e32 v105, v63, v105, vcc
	v_or_b32_e32 v105, v54, v105
	global_load_dwordx4 v[2:5], v105, s[4:5]
	global_load_dwordx4 v[6:9], v105, s[4:5] offset:64
	s_waitcnt vmcnt(9)
	v_cvt_pk_f32_fp8_e32 v[96:97], v10
	v_cvt_pk_f32_fp8_sdwa v[98:99], v10 src0_sel:WORD_1
	v_cvt_pk_f32_fp8_e32 v[100:101], v11
	v_cvt_pk_f32_fp8_sdwa v[102:103], v11 src0_sel:WORD_1
	v_pk_add_f32 v[88:89], v[88:89], v[96:97]
	v_pk_add_f32 v[90:91], v[90:91], v[98:99]
	v_pk_add_f32 v[92:93], v[92:93], v[100:101]
	v_pk_add_f32 v[94:95], v[94:95], v[102:103]
	v_cvt_pk_f32_fp8_e32 v[96:97], v12
	v_cvt_pk_f32_fp8_sdwa v[98:99], v12 src0_sel:WORD_1
	v_cvt_pk_f32_fp8_e32 v[100:101], v13
	v_cvt_pk_f32_fp8_sdwa v[102:103], v13 src0_sel:WORD_1
	v_pk_add_f32 v[76:77], v[76:77], v[96:97]
	v_pk_add_f32 v[80:81], v[80:81], v[98:99]
	v_pk_add_f32 v[84:85], v[84:85], v[100:101]
	v_pk_add_f32 v[86:87], v[86:87], v[102:103]
	v_cvt_pk_f32_fp8_e32 v[96:97], v14
	v_cvt_pk_f32_fp8_sdwa v[98:99], v14 src0_sel:WORD_1
	v_cvt_pk_f32_fp8_e32 v[100:101], v15
	v_cvt_pk_f32_fp8_sdwa v[102:103], v15 src0_sel:WORD_1
	v_pk_add_f32 v[72:73], v[72:73], v[96:97]
	v_pk_add_f32 v[74:75], v[74:75], v[98:99]
	v_pk_add_f32 v[78:79], v[78:79], v[100:101]
	v_pk_add_f32 v[82:83], v[82:83], v[102:103]
	v_cvt_pk_f32_fp8_e32 v[96:97], v16
	v_cvt_pk_f32_fp8_sdwa v[98:99], v16 src0_sel:WORD_1
	v_cvt_pk_f32_fp8_e32 v[100:101], v17
	v_cvt_pk_f32_fp8_sdwa v[102:103], v17 src0_sel:WORD_1
	v_pk_add_f32 v[64:65], v[64:65], v[96:97]
	v_pk_add_f32 v[66:67], v[66:67], v[98:99]
	v_pk_add_f32 v[68:69], v[68:69], v[100:101]
	v_pk_add_f32 v[70:71], v[70:71], v[102:103]
	v_add_u32_e32 v104, 7, v50
	v_cmp_lt_i32_e32 vcc, v104, v51
	v_lshlrev_b32_e32 v105, 7, v57
	s_nop 0
	v_cndmask_b32_e32 v105, v63, v105, vcc
	v_or_b32_e32 v105, v54, v105
	global_load_dwordx4 v[10:13], v105, s[4:5]
	global_load_dwordx4 v[14:17], v105, s[4:5] offset:64
	s_waitcnt vmcnt(11)
	v_cvt_pk_f32_fp8_e32 v[96:97], v18
	v_cvt_pk_f32_fp8_sdwa v[98:99], v18 src0_sel:WORD_1
	v_cvt_pk_f32_fp8_e32 v[100:101], v19
	v_cvt_pk_f32_fp8_sdwa v[102:103], v19 src0_sel:WORD_1
	v_pk_add_f32 v[88:89], v[88:89], v[96:97]
	v_pk_add_f32 v[90:91], v[90:91], v[98:99]
	v_pk_add_f32 v[92:93], v[92:93], v[100:101]
	v_pk_add_f32 v[94:95], v[94:95], v[102:103]
	v_cvt_pk_f32_fp8_e32 v[96:97], v20
	v_cvt_pk_f32_fp8_sdwa v[98:99], v20 src0_sel:WORD_1
	v_cvt_pk_f32_fp8_e32 v[100:101], v21
	v_cvt_pk_f32_fp8_sdwa v[102:103], v21 src0_sel:WORD_1
	v_pk_add_f32 v[76:77], v[76:77], v[96:97]
	v_pk_add_f32 v[80:81], v[80:81], v[98:99]
	v_pk_add_f32 v[84:85], v[84:85], v[100:101]
	v_pk_add_f32 v[86:87], v[86:87], v[102:103]
	v_cvt_pk_f32_fp8_e32 v[96:97], v22
	v_cvt_pk_f32_fp8_sdwa v[98:99], v22 src0_sel:WORD_1
	v_cvt_pk_f32_fp8_e32 v[100:101], v23
	v_cvt_pk_f32_fp8_sdwa v[102:103], v23 src0_sel:WORD_1
	v_pk_add_f32 v[72:73], v[72:73], v[96:97]
	v_pk_add_f32 v[74:75], v[74:75], v[98:99]
	v_pk_add_f32 v[78:79], v[78:79], v[100:101]
	v_pk_add_f32 v[82:83], v[82:83], v[102:103]
	v_cvt_pk_f32_fp8_e32 v[96:97], v24
	v_cvt_pk_f32_fp8_sdwa v[98:99], v24 src0_sel:WORD_1
	v_cvt_pk_f32_fp8_e32 v[100:101], v25
	v_cvt_pk_f32_fp8_sdwa v[102:103], v25 src0_sel:WORD_1
	v_pk_add_f32 v[64:65], v[64:65], v[96:97]
	v_pk_add_f32 v[66:67], v[66:67], v[98:99]
	v_pk_add_f32 v[68:69], v[68:69], v[100:101]
	v_pk_add_f32 v[70:71], v[70:71], v[102:103]
	v_add_u32_e32 v104, 8, v50
	v_cmp_lt_i32_e32 vcc, v104, v51
	v_lshlrev_b32_e32 v105, 7, v58
	s_nop 0
	v_cndmask_b32_e32 v105, v63, v105, vcc
	v_or_b32_e32 v105, v54, v105
	global_load_dwordx4 v[18:21], v105, s[4:5]
	global_load_dwordx4 v[22:25], v105, s[4:5] offset:64
	v_add_u32_e32 v106, 12, v50
	v_lshlrev_b32_e32 v106, 2, v106
	global_load_dwordx3 v[56:58], v106, s[8:9]
	s_waitcnt vmcnt(7)
	v_cvt_pk_f32_fp8_e32 v[96:97], v26
	v_cvt_pk_f32_fp8_sdwa v[98:99], v26 src0_sel:WORD_1
	v_cvt_pk_f32_fp8_e32 v[100:101], v27
	v_cvt_pk_f32_fp8_sdwa v[102:103], v27 src0_sel:WORD_1
	v_pk_add_f32 v[88:89], v[88:89], v[96:97]
	v_pk_add_f32 v[90:91], v[90:91], v[98:99]
	v_pk_add_f32 v[92:93], v[92:93], v[100:101]
	v_pk_add_f32 v[94:95], v[94:95], v[102:103]
	v_cvt_pk_f32_fp8_e32 v[96:97], v28
	v_cvt_pk_f32_fp8_sdwa v[98:99], v28 src0_sel:WORD_1
	v_cvt_pk_f32_fp8_e32 v[100:101], v29
	v_cvt_pk_f32_fp8_sdwa v[102:103], v29 src0_sel:WORD_1
	v_pk_add_f32 v[76:77], v[76:77], v[96:97]
	v_pk_add_f32 v[80:81], v[80:81], v[98:99]
	v_pk_add_f32 v[84:85], v[84:85], v[100:101]
	v_pk_add_f32 v[86:87], v[86:87], v[102:103]
	v_cvt_pk_f32_fp8_e32 v[96:97], v30
	v_cvt_pk_f32_fp8_sdwa v[98:99], v30 src0_sel:WORD_1
	v_cvt_pk_f32_fp8_e32 v[100:101], v31
	v_cvt_pk_f32_fp8_sdwa v[102:103], v31 src0_sel:WORD_1
	v_pk_add_f32 v[72:73], v[72:73], v[96:97]
	v_pk_add_f32 v[74:75], v[74:75], v[98:99]
	v_pk_add_f32 v[78:79], v[78:79], v[100:101]
	v_pk_add_f32 v[82:83], v[82:83], v[102:103]
	v_cvt_pk_f32_fp8_e32 v[96:97], v32
	v_cvt_pk_f32_fp8_sdwa v[98:99], v32 src0_sel:WORD_1
	v_cvt_pk_f32_fp8_e32 v[100:101], v33
	v_cvt_pk_f32_fp8_sdwa v[102:103], v33 src0_sel:WORD_1
	v_pk_add_f32 v[64:65], v[64:65], v[96:97]
	v_pk_add_f32 v[66:67], v[66:67], v[98:99]
	v_pk_add_f32 v[68:69], v[68:69], v[100:101]
	v_pk_add_f32 v[70:71], v[70:71], v[102:103]
	v_add_u32_e32 v104, 9, v50
	v_cmp_lt_i32_e32 vcc, v104, v51
	v_lshlrev_b32_e32 v105, 7, v60
	s_nop 0
	v_cndmask_b32_e32 v105, v63, v105, vcc
	v_or_b32_e32 v105, v54, v105
	global_load_dwordx4 v[26:29], v105, s[4:5]
	global_load_dwordx4 v[30:33], v105, s[4:5] offset:64
	s_waitcnt vmcnt(9)
	v_cvt_pk_f32_fp8_e32 v[96:97], v34
	v_cvt_pk_f32_fp8_sdwa v[98:99], v34 src0_sel:WORD_1
	v_cvt_pk_f32_fp8_e32 v[100:101], v35
	v_cvt_pk_f32_fp8_sdwa v[102:103], v35 src0_sel:WORD_1
	v_pk_add_f32 v[88:89], v[88:89], v[96:97]
	v_pk_add_f32 v[90:91], v[90:91], v[98:99]
	v_pk_add_f32 v[92:93], v[92:93], v[100:101]
	v_pk_add_f32 v[94:95], v[94:95], v[102:103]
	v_cvt_pk_f32_fp8_e32 v[96:97], v36
	v_cvt_pk_f32_fp8_sdwa v[98:99], v36 src0_sel:WORD_1
	v_cvt_pk_f32_fp8_e32 v[100:101], v37
	v_cvt_pk_f32_fp8_sdwa v[102:103], v37 src0_sel:WORD_1
	v_pk_add_f32 v[76:77], v[76:77], v[96:97]
	v_pk_add_f32 v[80:81], v[80:81], v[98:99]
	v_pk_add_f32 v[84:85], v[84:85], v[100:101]
	v_pk_add_f32 v[86:87], v[86:87], v[102:103]
	v_cvt_pk_f32_fp8_e32 v[96:97], v38
	v_cvt_pk_f32_fp8_sdwa v[98:99], v38 src0_sel:WORD_1
	v_cvt_pk_f32_fp8_e32 v[100:101], v39
	v_cvt_pk_f32_fp8_sdwa v[102:103], v39 src0_sel:WORD_1
	v_pk_add_f32 v[72:73], v[72:73], v[96:97]
	v_pk_add_f32 v[74:75], v[74:75], v[98:99]
	v_pk_add_f32 v[78:79], v[78:79], v[100:101]
	v_pk_add_f32 v[82:83], v[82:83], v[102:103]
	v_cvt_pk_f32_fp8_e32 v[96:97], v40
	v_cvt_pk_f32_fp8_sdwa v[98:99], v40 src0_sel:WORD_1
	v_cvt_pk_f32_fp8_e32 v[100:101], v41
	v_cvt_pk_f32_fp8_sdwa v[102:103], v41 src0_sel:WORD_1
	v_pk_add_f32 v[64:65], v[64:65], v[96:97]
	v_pk_add_f32 v[66:67], v[66:67], v[98:99]
	v_pk_add_f32 v[68:69], v[68:69], v[100:101]
	v_pk_add_f32 v[70:71], v[70:71], v[102:103]
	v_add_u32_e32 v104, 10, v50
	v_cmp_lt_i32_e32 vcc, v104, v51
	v_lshlrev_b32_e32 v105, 7, v61
	s_nop 0
	v_cndmask_b32_e32 v105, v63, v105, vcc
	v_or_b32_e32 v105, v54, v105
	global_load_dwordx4 v[34:37], v105, s[4:5]
	global_load_dwordx4 v[38:41], v105, s[4:5] offset:64
	s_waitcnt vmcnt(11)
	v_cvt_pk_f32_fp8_e32 v[96:97], v42
	v_cvt_pk_f32_fp8_sdwa v[98:99], v42 src0_sel:WORD_1
	v_cvt_pk_f32_fp8_e32 v[100:101], v43
	v_cvt_pk_f32_fp8_sdwa v[102:103], v43 src0_sel:WORD_1
	v_pk_add_f32 v[88:89], v[88:89], v[96:97]
	v_pk_add_f32 v[90:91], v[90:91], v[98:99]
	v_pk_add_f32 v[92:93], v[92:93], v[100:101]
	v_pk_add_f32 v[94:95], v[94:95], v[102:103]
	v_cvt_pk_f32_fp8_e32 v[96:97], v44
	v_cvt_pk_f32_fp8_sdwa v[98:99], v44 src0_sel:WORD_1
	v_cvt_pk_f32_fp8_e32 v[100:101], v45
	v_cvt_pk_f32_fp8_sdwa v[102:103], v45 src0_sel:WORD_1
	v_pk_add_f32 v[76:77], v[76:77], v[96:97]
	v_pk_add_f32 v[80:81], v[80:81], v[98:99]
	v_pk_add_f32 v[84:85], v[84:85], v[100:101]
	v_pk_add_f32 v[86:87], v[86:87], v[102:103]
	v_cvt_pk_f32_fp8_e32 v[96:97], v46
	v_cvt_pk_f32_fp8_sdwa v[98:99], v46 src0_sel:WORD_1
	v_cvt_pk_f32_fp8_e32 v[100:101], v47
	v_cvt_pk_f32_fp8_sdwa v[102:103], v47 src0_sel:WORD_1
	v_pk_add_f32 v[72:73], v[72:73], v[96:97]
	v_pk_add_f32 v[74:75], v[74:75], v[98:99]
	v_pk_add_f32 v[78:79], v[78:79], v[100:101]
	v_pk_add_f32 v[82:83], v[82:83], v[102:103]
	v_cvt_pk_f32_fp8_e32 v[96:97], v48
	v_cvt_pk_f32_fp8_sdwa v[98:99], v48 src0_sel:WORD_1
	v_cvt_pk_f32_fp8_e32 v[100:101], v49
	v_cvt_pk_f32_fp8_sdwa v[102:103], v49 src0_sel:WORD_1
	v_pk_add_f32 v[64:65], v[64:65], v[96:97]
	v_pk_add_f32 v[66:67], v[66:67], v[98:99]
	v_pk_add_f32 v[68:69], v[68:69], v[100:101]
	v_pk_add_f32 v[70:71], v[70:71], v[102:103]
	v_add_u32_e32 v104, 11, v50
	v_cmp_lt_i32_e32 vcc, v104, v51
	v_lshlrev_b32_e32 v105, 7, v62
	s_nop 0
	v_cndmask_b32_e32 v105, v63, v105, vcc
	v_or_b32_e32 v105, v54, v105
	global_load_dwordx4 v[42:45], v105, s[4:5]
	global_load_dwordx4 v[46:49], v105, s[4:5] offset:64
	v_add_u32_e32 v106, 15, v50
	v_lshlrev_b32_e32 v106, 2, v106
	global_load_dwordx3 v[60:62], v106, s[8:9]
	v_add_u32_e32 v50, 6, v50
	v_add_u32_e32 v104, 6, v50
	v_cmp_lt_i32_e32 vcc, v104, v51
	s_and_b64 vcc, exec, vcc
	s_cbranch_scc1 .Lagg_gloop
